# baseline (speedup 1.0000x reference)
_Z9feat_gemmPKDF16_S0_PDF16_:
	s_load_dwordx4 s[4:7], s[0:1], 0x8
	s_load_dwordx2 s[8:9], s[0:1], 0x0
	s_lshr_b32 s10, s2, 6
	s_lshl_b32 s10, s10, 3
	s_and_b32 s11, s2, 7
	s_or_b32 s10, s10, s11
	s_bfe_u32 s11, s2, 0x30003
	s_mul_i32 s12, s10, 0x44
	s_lshr_b32 s14, s12, 4
	s_lshl_b32 s15, s14, 3
	s_sub_u32 s15, 0x441, s15
	v_cvt_f32_u32_e32 v174, s15
	v_sqrt_f32_e32 v174, v174
	v_and_b32_e32 v170, 63, v0
	v_lshrrev_b32_e32 v171, 6, v0
	v_sub_f32_e32 v174, 0x42040000, v174
	v_fmaak_f32 v174, 0.5, v174, 0x3c23d70a
	v_cvt_u32_f32_e32 v174, v174
	v_lshlrev_b32_e32 v160, 4, v170
	v_readfirstlane_b32 s13, v174
	s_sub_u32 s15, 33, s13
	s_mul_i32 s15, s15, s13
	s_lshr_b32 s15, s15, 1
	s_sub_u32 s14, s14, s15
	s_add_u32 s14, s14, s13
	s_bfe_u32 s46, s12, 0x20002
	v_and_b32_e32 v172, 31, v170
	v_readfirstlane_b32 s33, v171
	v_lshrrev_b32_e32 v173, 5, v170
	s_lshl_b32 s35, s33, 11
	s_lshl_b32 s34, s11, 8
	s_lshl_b32 s36, s33, 5
	s_add_u32 s34, s34, s36
	v_add_lshl_u32 v165, v172, s34, 4
	v_add_u32_e32 v166, 0x8000, v165
	v_lshl_add_u32 v164, v173, 15, v165
	v_add_u32_e32 v168, s35, v160
	v_mov_b32_e32 v161, v160
	s_waitcnt lgkmcnt(0)
	s_lshl_b32 s36, s12, 12
	s_add_u32 s20, s4, s36
	s_addc_u32 s21, s5, 0
	s_mov_b32 s17, 0
	s_mov_b32 s18, 0
	s_mov_b32 s19, 0
	s_mov_b32 s22, 0
	s_sub_u32 s39, 5, s46
	s_mov_b32 s38, 2
	s_cmp_le_u32 s22, 16
	s_cselect_b32 s40, s18, 0x18000
	s_add_u32 m0, s40, s35
	s_add_u32 s22, s22, 1
	global_load_lds_dwordx4 v168, s[20:21]
	global_load_lds_dwordx4 v168, s[20:21] offset:1024
	s_cmp_le_u32 s22, 16
	s_cselect_b32 s41, 0x4000, 0
	s_add_u32 s20, s20, s41
	s_addc_u32 s21, s21, 0
	s_add_u32 s18, s18, 0x4000
	s_cmp_eq_u32 s18, 0x18000
	s_cselect_b32 s18, 0, s18
	s_cmp_le_u32 s22, 16
	s_cselect_b32 s40, s18, 0x18000
	s_add_u32 m0, s40, s35
	s_add_u32 s22, s22, 1
	global_load_lds_dwordx4 v168, s[20:21]
	global_load_lds_dwordx4 v168, s[20:21] offset:1024
	s_cmp_le_u32 s22, 16
	s_cselect_b32 s41, 0x4000, 0
	s_add_u32 s20, s20, s41
	s_addc_u32 s21, s21, 0
	s_add_u32 s18, s18, 0x4000
	s_cmp_eq_u32 s18, 0x18000
	s_cselect_b32 s18, 0, s18
	s_min_u32 s43, s13, 15
	s_min_u32 s44, s14, 15
	s_lshl_b32 s45, s44, 16
	s_add_u32 s24, s8, s45
	s_addc_u32 s25, s9, 0
	s_add_u32 s26, s24, 0x100000
	s_addc_u32 s27, s25, 0
	s_lshl_b32 s45, s43, 16
	s_add_u32 s28, s8, s45
	s_addc_u32 s29, s9, 0
	s_add_u32 s30, s28, 0x100000
	s_addc_u32 s31, s29, 0
	global_load_dwordx4 v[36:39], v164, s[24:25]
	global_load_dwordx4 v[32:35], v164, s[26:27]
	global_load_dwordx4 v[40:43], v165, s[28:29]
	global_load_dwordx4 v[44:47], v166, s[28:29]
	global_load_dwordx4 v[48:51], v165, s[30:31]
	global_load_dwordx4 v[52:55], v166, s[30:31]
